# diff attention far tiles: second-map K/Q LDS fragments prefetched into the (free in far tiles) bias registers at tile start
# baseline (speedup 1.0000x reference)
; #define LAS __attribute__((address_space(3)))
; __device__ __forceinline__ void diff_tile(const bool near, const LAS unsigned char* Kb, const LAS unsigned char* Vb, const LAS float* btab, const LAS bf16x8* Qs, f32x16 (&O)[2][2],
;                                           float (&lsum)[2], int qpos, int k0, int l31, int hi, float c2, float farraw) {
;     ...
;     for (int c = 0; c < 2; ++c) {
;         f32x16 S[2];
; #pragma unroll
;         for (int kb = 0; kb < 2; ++kb) {
;             f32x16 acc;
; #pragma unroll
;             for (int r = 0; r < 16; ++r) acc[r] = 0.f;
; #pragma unroll
;             for (int s = 0; s < 2; ++s) { const bf16x8 kf = *(const LAS bf16x8*)(Kb + (32 * kb + l31) * DF_PITCH + c * 64 + s * 32 + hi * 16);
;                 acc = __builtin_amdgcn_mfma_f32_32x32x16_bf16(kf, Qs[(c * 2 + s) * 64], acc, 0, 0, 0); }
;             acc = __builtin_amdgcn_mfma_f32_32x32x16_bf16(kx, Qs[(4 + c) * 64], acc, 0, 0, 0);
;             S[kb] = acc;
;         }
;         if (near) {
; #pragma unroll
;             for (int kb = 0; kb < 2; ++kb)
; #pragma unroll
;                 for (int r = 0; r < 16; ++r) S[kb][r] += bm[kb][r]; }
;         float ls = 0.f;
;         bf16x8 Pf[4];
; #pragma unroll
;         for (int kb = 0; kb < 2; ++kb) {
; #pragma unroll
;             for (int r = 0; r < 16; ++r) { const float pv = __builtin_amdgcn_exp2f(S[kb][r]); ls += pv; S[kb][r] = pv; }
; #pragma unroll
;             for (int s = 0; s < 2; ++s) Pf[2 * kb + s] = pack_acc(S[kb], s);
;         }
;         lsum[c] += ls;
; #pragma unroll
;         for (int st = 0; st < 4; ++st)
; #pragma unroll
;             for (int dvb = 0; dvb < 2; ++dvb) O[c][dvb] = __builtin_amdgcn_mfma_f32_32x32x16_bf16(Vf[st][dvb], Pf[st], O[c][dvb], 0, 0, 0);
;     }
.Ldf_far_e0:
	ds_read_b128 v[152:155], v193 offset:4160
	ds_read_b128 v[156:159], v189 offset:43008
	ds_read_b128 v[160:163], v193 offset:4192
	ds_read_b128 v[164:167], v189 offset:44032
	ds_read_b128 v[168:171], v193 offset:8768
	ds_read_b128 v[172:175], v193 offset:8800
	ds_read_b128 v[176:179], v189 offset:46080
	s_nop 9
	v_exp_f32_e32 v194, v82
	v_exp_f32_e32 v195, v83
	v_exp_f32_e32 v196, v84
	v_exp_f32_e32 v197, v85
	v_exp_f32_e32 v198, v86
	v_exp_f32_e32 v199, v87
	v_exp_f32_e32 v223, v88
	v_exp_f32_e32 v224, v89
	v_cvt_pk_bf16_f32 v82, v194, v195
	v_cvt_pk_bf16_f32 v83, v196, v197
	v_cvt_pk_bf16_f32 v84, v198, v199
	v_cvt_pk_bf16_f32 v85, v223, v224
	v_exp_f32_e32 v225, v90
	v_exp_f32_e32 v226, v91
	s_waitcnt lgkmcnt(14)
	v_mfma_f32_32x32x16_bf16 v[50:65], v[138:141], v[82:85], v[50:65]
	v_exp_f32_e32 v227, v92
	v_exp_f32_e32 v228, v93
	v_exp_f32_e32 v229, v94
	v_exp_f32_e32 v230, v95
	v_exp_f32_e32 v231, v96
	v_exp_f32_e32 v232, v97
	v_exp_f32_e32 v233, v66
	s_waitcnt lgkmcnt(9)
	v_mfma_f32_32x32x16_bf16 v[18:33], v[134:137], v[82:85], v[18:33]
	v_cvt_pk_bf16_f32 v82, v225, v226
	v_cvt_pk_bf16_f32 v83, v227, v228
	v_cvt_pk_bf16_f32 v84, v229, v230
	v_cvt_pk_bf16_f32 v85, v231, v232
	v_exp_f32_e32 v234, v67
	v_exp_f32_e32 v235, v68
	v_exp_f32_e32 v236, v69
	v_mfma_f32_32x32x16_bf16 v[50:65], v[130:133], v[82:85], v[50:65]
	v_exp_f32_e32 v237, v70
	v_exp_f32_e32 v238, v71
	v_exp_f32_e32 v239, v72
	v_exp_f32_e32 v240, v73
	v_cvt_pk_bf16_f32 v66, v233, v234
	v_cvt_pk_bf16_f32 v67, v235, v236
	v_cvt_pk_bf16_f32 v68, v237, v238
	v_mfma_f32_32x32x16_bf16 v[18:33], v[126:129], v[82:85], v[18:33]
	v_cvt_pk_bf16_f32 v69, v239, v240
	v_exp_f32_e32 v241, v74
	v_exp_f32_e32 v242, v75
	v_exp_f32_e32 v243, v76
	v_exp_f32_e32 v244, v77
	v_exp_f32_e32 v245, v78
	v_exp_f32_e32 v246, v79
	v_mfma_f32_32x32x16_bf16 v[50:65], v[122:125], v[66:69], v[50:65]
	v_exp_f32_e32 v247, v80
	v_exp_f32_e32 v248, v81
	s_and_b64 vcc, exec, s[0:1]
	v_mfma_f32_32x32x16_bf16 v[18:33], v[118:121], v[66:69], v[18:33]
	v_cvt_pk_bf16_f32 v66, v241, v242
	v_cvt_pk_bf16_f32 v67, v243, v244
	v_cvt_pk_bf16_f32 v68, v245, v246
	v_cvt_pk_bf16_f32 v69, v247, v248
	s_waitcnt lgkmcnt(8)
	s_nop 0
	v_mfma_f32_32x32x16_bf16 v[50:65], v[114:117], v[66:69], v[50:65]
	s_waitcnt lgkmcnt(7)
	v_mfma_f32_32x32x16_bf16 v[18:33], v[110:113], v[66:69], v[18:33]
	s_waitcnt lgkmcnt(5)
	v_mfma_f32_32x32x16_bf16 v[82:97], v[152:155], v[156:159], 0
	s_waitcnt lgkmcnt(3)
	v_mfma_f32_32x32x16_bf16 v[82:97], v[160:163], v[164:167], v[82:97]
	s_waitcnt lgkmcnt(2)
	v_mfma_f32_32x32x16_bf16 v[66:81], v[168:171], v[156:159], 0
	s_waitcnt lgkmcnt(1)
	v_mfma_f32_32x32x16_bf16 v[66:81], v[172:175], v[164:167], v[66:81]
	s_waitcnt lgkmcnt(0)
	v_mfma_f32_32x32x16_bf16 v[82:97], v[98:101], v[176:179], v[82:97]
	v_mfma_f32_32x32x16_bf16 v[66:81], v[98:101], v[176:179], v[66:81]
	s_branch .LBB0_790
